# v7: gate epilogue regenerated (packed math, prefetch) + layer-0 gate tile rebalance across workgroups
# speedup vs baseline: 1.0277x; 1.0163x over previous
; __device__ __forceinline__ size_t gate_tile_off(int pm, int pg, int wr, int wc, int fr, int fq) { return ((size_t)pm * 12 + pg) * 65536 + (size_t)(wr * 4 + wc) * 1024 + (size_t)(fq * 16 + fr) * 16; }
;     __device__ __forceinline__ bool next(int i, pg8::Unit& u) const {
;         const long L = (long)i * G + c; if (L >= count) return false;
;         pg8::tile_order((int)L + base, nM, nN, u.pm, u.pn); u.sub = 0;
;         u.a = A + (size_t)u.pm * 256 * K * 2; u.b = Bt + (size_t)u.pn * 256 * K * 2; return true;
;     __device__ __forceinline__ void operator()(const pg8::i32x4 (&acc)[2][2][4][2], const pg8::Unit& u, int wr, int wc, int fr, int fq) const {
;         unsigned char* G = ws + AR_G + gate_tile_off(u.pm, u.pn, wr, wc, fr, fq); const float* rs = (const float*)(ws + WS_RSQA);
;         const int col0 = u.pn * 256 + wc * 32 + 8 * fq;
;         const float* cp = (const float*)(ws + CTL_AMAX) + AMAX_GATE + l * INC + col0; const float* bp = P.in[5] + l * 3 * D + col0;
;         float rsv[2][4];
; #pragma unroll
;         for (int ai = 0; ai < 2; ++ai)
; #pragma unroll
;             for (int m = 0; m < 4; ++m) rsv[ai][m] = rs[u.pm * 256 + ai * 128 + wr * 64 + m * 16 + fr];
;         f32x4 cs[2][2], bg[2][2];
; #pragma unroll
;         for (int bj = 0; bj < 2; ++bj)
; #pragma unroll
;             for (int n = 0; n < 2; ++n) { cs[bj][n] = *(const f32x4*)(cp + 128 * bj + 4 * n) * (1.0f / 127.0f); bg[bj][n] = *(const f32x4*)(bp + 128 * bj + 4 * n); }
.LBB0_443:
	s_lshl_b32 s2, s51, 8
	v_mbcnt_lo_u32_b32 v246, -1, 0
	s_or_b32 s2, s2, s46
	v_mbcnt_hi_u32_b32 v246, -1, v246
	s_lshl_b32 s3, s20, 8
	v_lshrrev_b32_e32 v247, 1, v246
	s_add_i32 s3, s3, s45
	v_and_b32_e32 v247, 24, v247
	v_and_or_b32 v246, v246, 15, s3
	v_add_u32_e32 v247, s2, v247
	v_lshlrev_b32_e32 v246, 2, v246
	v_lshlrev_b32_e32 v247, 2, v247
	global_load_dwordx4 v[206:209], v247, s[10:11]
	global_load_dwordx4 v[210:213], v247, s[10:11] offset:16
	global_load_dwordx4 v[214:217], v247, s[10:11] offset:512
	global_load_dwordx4 v[218:221], v247, s[10:11] offset:528
	global_load_dwordx4 v[222:225], v247, s[8:9]
	global_load_dwordx4 v[226:229], v247, s[8:9] offset:16
	global_load_dwordx4 v[230:233], v247, s[8:9] offset:512
	global_load_dwordx4 v[234:237], v247, s[8:9] offset:528
	global_load_dword v238, v246, s[38:39]
	global_load_dword v239, v246, s[38:39] offset:64
	global_load_dword v240, v246, s[38:39] offset:128
	global_load_dword v241, v246, s[38:39] offset:192
	global_load_dword v242, v246, s[38:39] offset:512
	global_load_dword v243, v246, s[38:39] offset:576
	global_load_dword v244, v246, s[38:39] offset:640
	global_load_dword v245, v246, s[38:39] offset:704
	s_add_i32 s33, s33, 1
	s_mul_i32 s2, s33, s95
	s_mul_hi_u32 s3, s33, s78
	s_add_i32 s3, s3, s2
	s_mul_i32 s2, s33, s78
	s_add_u32 s26, s2, s64
	s_addc_u32 s27, s3, s41
	s_cmp_eq_u32 s34, 0
	s_cbranch_scc1 .Lgsched_done
	s_cmp_lt_u32 s64, 0x80
	s_cbranch_scc1 .Lgsched_done
	s_cmp_lt_u32 s64, 0xc0
	s_cbranch_scc0 .Lgsched_hi
	s_cmp_eq_u32 s33, 5
	s_cbranch_scc0 .Lgsched_done
	s_movk_i32 s26, 0x600
	s_mov_b32 s27, 0
	s_branch .Lgsched_done
.Lgsched_hi:
	s_cmp_eq_u32 s33, 6
	s_cbranch_scc0 .Lgsched_done
	s_add_i32 s26, s64, 0x4c0
	s_mov_b32 s27, 0
.Lgsched_done:
	v_mov_b64_e32 v[0:1], 0x600
	v_cmp_lt_i64_e64 s[2:3], s[26:27], v[0:1]
	v_mov_b64_e32 v[0:1], 0x5ff
	v_cmp_gt_i64_e32 vcc, s[26:27], v[0:1]
	s_cbranch_vccnz .LBB0_445
	s_ashr_i32 s12, s26, 31
	s_lshr_b32 s12, s12, 29
	s_add_i32 s12, s26, s12
	s_ashr_i32 s13, s12, 3
	s_and_b32 s12, s12, -8
	s_sub_i32 s12, s26, s12
	s_cmp_lt_i32 s12, 0
	s_movk_i32 s4, 0xc1
	s_cselect_b32 s14, s4, 0xc0
	s_mul_i32 s12, s12, s14
	s_add_i32 s12, s12, s13
	s_mul_hi_i32 s13, s12, 0x2aaaaaab
	s_lshr_b32 s14, s13, 31
	s_ashr_i32 s13, s13, 3
	s_add_i32 s13, s13, s14
	s_lshl_b32 s14, s13, 2
	s_sub_i32 s15, 0x80, s14
	s_min_i32 s15, s15, 4
	s_abs_i32 s16, s15
	v_cvt_f32_u32_e32 v0, s16
	s_sub_i32 s18, 0, s16
	s_mul_i32 s13, s13, 48
	s_sub_i32 s13, s12, s13
	v_rcp_iflag_f32_e32 v0, v0
	s_abs_i32 s12, s13
	s_xor_b32 s17, s13, s15
	s_ashr_i32 s17, s17, 31
	v_mul_f32_e32 v0, 0x4f7ffffe, v0
	v_cvt_u32_f32_e32 v0, v0
	s_nop 0
	v_readfirstlane_b32 s19, v0
	s_mul_i32 s18, s18, s19
	s_mul_hi_u32 s18, s19, s18
	s_add_i32 s19, s19, s18
	s_mul_hi_u32 s18, s12, s19
	s_mul_i32 s19, s18, s16
	s_sub_i32 s12, s12, s19
	s_add_i32 s26, s18, 1
	s_sub_i32 s19, s12, s16
	s_cmp_ge_u32 s12, s16
	s_cselect_b32 s18, s26, s18
	s_cselect_b32 s12, s19, s12
	s_add_i32 s19, s18, 1
	s_cmp_ge_u32 s12, s16
	s_cselect_b32 s12, s19, s18
	s_xor_b32 s12, s12, s17
	s_sub_i32 s12, s12, s17
	s_mul_i32 s15, s12, s15
	s_sub_i32 s13, s13, s15
	s_add_i32 s14, s14, s13
	s_ashr_i32 s15, s14, 31
	s_lshl_b64 s[16:17], s[14:15], 18
	s_add_u32 s16, s65, s16
	s_addc_u32 s17, s68, s17
	s_ashr_i32 s13, s12, 31
	s_lshl_b64 s[18:19], s[12:13], 18
	s_add_u32 s18, s30, s18
	s_addc_u32 s19, s31, s19

; __device__ __forceinline__ float sigmoidf_fast(float x) { return fast_rcp(1.0f + fast_exp2(-x * LOG2E)); }
; #define ROW_FENCE() asm volatile("" ::: "memory")
;     __device__ __forceinline__ void operator()(const pg8::i32x4 (&acc)[2][2][4][2], const pg8::Unit& u, int wr, int wc, int fr, int fq) const {
;     ...
;         f32x4 cs[2][2], bg[2][2];
; #pragma unroll
;         for (int bj = 0; bj < 2; ++bj)
; #pragma unroll
;             for (int n = 0; n < 2; ++n) { cs[bj][n] = *(const f32x4*)(cp + 128 * bj + 4 * n) * (1.0f / 127.0f); bg[bj][n] = *(const f32x4*)(bp + 128 * bj + 4 * n); }
; #pragma unroll
;         for (int ai = 0; ai < 2; ++ai)
; #pragma unroll
;             for (int m = 0; m < 4; ++m) {
;                 const int row = u.pm * 256 + ai * 128 + wr * 64 + m * 16 + fr; const float r = rsv[ai][m];
;                 u32x4 gq = {0u, 0u, 0u, 0u};
; #pragma unroll
;                 for (int bj = 0; bj < 2; ++bj)
; #pragma unroll
;                     for (int n = 0; n < 2; ++n)
; #pragma unroll
;                         for (int j = 0; j < 4; ++j) gq[2 * bj + n] = __builtin_amdgcn_cvt_pk_u8_f32(fmaxf(__builtin_rintf(sigmoidf_fast((float)acc[ai][bj][m][n][j] * (r * cs[bj][n][j]) + bg[bj][n][j]) * 255.0f), 1.0f), j, gq[2 * bj + n]);
;                 if (!dry) *(u32x4*)(G + (ai * 4 + m) * 8192) = gq;
;                 ROW_FENCE();
.LBB0_449:
	v_mbcnt_lo_u32_b32 v154, -1, 0
	v_mbcnt_hi_u32_b32 v154, -1, v154
	s_mul_i32 s13, s20, 12
	s_add_i32 s13, s13, s51
	s_lshl_b32 s13, s13, 16
	s_add_u32 s22, s49, s13
	s_addc_u32 s23, s50, 0
	v_lshlrev_b32_e32 v152, 4, v154
	s_waitcnt vmcnt(8)
	s_mov_b32 s4, 0xbc3a1e78
	v_pk_mul_f32 v[206:207], v[206:207], s[4:5] op_sel_hi:[1,0]
	v_pk_mul_f32 v[208:209], v[208:209], s[4:5] op_sel_hi:[1,0]
	v_pk_mul_f32 v[210:211], v[210:211], s[4:5] op_sel_hi:[1,0]
	v_pk_mul_f32 v[212:213], v[212:213], s[4:5] op_sel_hi:[1,0]
	v_pk_mul_f32 v[214:215], v[214:215], s[4:5] op_sel_hi:[1,0]
	v_pk_mul_f32 v[216:217], v[216:217], s[4:5] op_sel_hi:[1,0]
	v_pk_mul_f32 v[218:219], v[218:219], s[4:5] op_sel_hi:[1,0]
	v_pk_mul_f32 v[220:221], v[220:221], s[4:5] op_sel_hi:[1,0]
	s_mov_b32 s4, 0xbfb8aa3b
	v_pk_mul_f32 v[222:223], v[222:223], s[4:5] op_sel_hi:[1,0]
	v_pk_mul_f32 v[224:225], v[224:225], s[4:5] op_sel_hi:[1,0]
	v_pk_mul_f32 v[226:227], v[226:227], s[4:5] op_sel_hi:[1,0]
	v_pk_mul_f32 v[228:229], v[228:229], s[4:5] op_sel_hi:[1,0]
	v_pk_mul_f32 v[230:231], v[230:231], s[4:5] op_sel_hi:[1,0]
	v_pk_mul_f32 v[232:233], v[232:233], s[4:5] op_sel_hi:[1,0]
	v_pk_mul_f32 v[234:235], v[234:235], s[4:5] op_sel_hi:[1,0]
	v_pk_mul_f32 v[236:237], v[236:237], s[4:5] op_sel_hi:[1,0]
	v_mov_b32_e32 v156, 0x3b808081
	v_cvt_f32_i32_e32 v138, v138
	v_cvt_f32_i32_e32 v139, v139
	v_cvt_f32_i32_e32 v140, v140
	v_cvt_f32_i32_e32 v141, v141
	v_cvt_f32_i32_e32 v134, v134
	v_cvt_f32_i32_e32 v135, v135
	v_cvt_f32_i32_e32 v136, v136
	v_cvt_f32_i32_e32 v137, v137
	v_pk_mul_f32 v[138:139], v[138:139], v[206:207]
	v_pk_mul_f32 v[140:141], v[140:141], v[208:209]
	v_pk_mul_f32 v[134:135], v[134:135], v[210:211]
	v_pk_mul_f32 v[136:137], v[136:137], v[212:213]
	v_pk_fma_f32 v[138:139], v[138:139], v[238:239], v[222:223] op_sel_hi:[1,0,1]
	v_pk_fma_f32 v[140:141], v[140:141], v[238:239], v[224:225] op_sel_hi:[1,0,1]
	v_pk_fma_f32 v[134:135], v[134:135], v[238:239], v[226:227] op_sel_hi:[1,0,1]
	v_pk_fma_f32 v[136:137], v[136:137], v[238:239], v[228:229] op_sel_hi:[1,0,1]
	v_exp_f32_e32 v138, v138
	v_exp_f32_e32 v139, v139
	v_exp_f32_e32 v140, v140
	v_exp_f32_e32 v141, v141
	v_exp_f32_e32 v134, v134
	v_exp_f32_e32 v135, v135
	v_exp_f32_e32 v136, v136
	v_exp_f32_e32 v137, v137
	v_pk_fma_f32 v[138:139], v[138:139], v[156:157], v[156:157] op_sel_hi:[1,0,0]
	v_pk_fma_f32 v[140:141], v[140:141], v[156:157], v[156:157] op_sel_hi:[1,0,0]
	v_pk_fma_f32 v[134:135], v[134:135], v[156:157], v[156:157] op_sel_hi:[1,0,0]
	v_pk_fma_f32 v[136:137], v[136:137], v[156:157], v[156:157] op_sel_hi:[1,0,0]
	v_rcp_f32_e32 v138, v138
	v_rcp_f32_e32 v139, v139
	v_rcp_f32_e32 v140, v140
	v_rcp_f32_e32 v141, v141
	v_rcp_f32_e32 v134, v134
	v_rcp_f32_e32 v135, v135
	v_rcp_f32_e32 v136, v136
	v_rcp_f32_e32 v137, v137
	v_mov_b32_e32 v153, v152
	v_rndne_f32_e32 v138, v138
	v_rndne_f32_e32 v139, v139
	v_rndne_f32_e32 v140, v140
	v_rndne_f32_e32 v141, v141
	v_rndne_f32_e32 v134, v134
	v_rndne_f32_e32 v135, v135
	v_rndne_f32_e32 v136, v136
	v_rndne_f32_e32 v137, v137
	v_max_f32_e32 v138, 1.0, v138
	v_max_f32_e32 v139, 1.0, v139
	v_max_f32_e32 v140, 1.0, v140
	v_max_f32_e32 v141, 1.0, v141
	v_max_f32_e32 v134, 1.0, v134
	v_max_f32_e32 v135, 1.0, v135
	v_max_f32_e32 v136, 1.0, v136
	v_max_f32_e32 v137, 1.0, v137
	v_cvt_pk_u8_f32 v144, v138, 0, 0
	v_cvt_pk_u8_f32 v145, v134, 0, 0
	v_cvt_pk_u8_f32 v144, v139, 1, v144
	v_cvt_pk_u8_f32 v145, v135, 1, v145
	v_cvt_pk_u8_f32 v144, v140, 2, v144
	v_cvt_pk_u8_f32 v145, v136, 2, v145
	v_cvt_pk_u8_f32 v144, v141, 3, v144
	v_cvt_pk_u8_f32 v145, v137, 3, v145
	v_cvt_f32_i32_e32 v130, v130
	v_cvt_f32_i32_e32 v131, v131
	v_cvt_f32_i32_e32 v132, v132
	v_cvt_f32_i32_e32 v133, v133
	v_cvt_f32_i32_e32 v60, v60
	v_cvt_f32_i32_e32 v61, v61
	v_cvt_f32_i32_e32 v62, v62
	v_cvt_f32_i32_e32 v63, v63
	v_pk_mul_f32 v[130:131], v[130:131], v[214:215]
	v_pk_mul_f32 v[132:133], v[132:133], v[216:217]
	v_pk_mul_f32 v[60:61], v[60:61], v[218:219]
	v_pk_mul_f32 v[62:63], v[62:63], v[220:221]
	v_pk_fma_f32 v[130:131], v[130:131], v[238:239], v[230:231] op_sel_hi:[1,0,1]
	v_pk_fma_f32 v[132:133], v[132:133], v[238:239], v[232:233] op_sel_hi:[1,0,1]
	v_pk_fma_f32 v[60:61], v[60:61], v[238:239], v[234:235] op_sel_hi:[1,0,1]
	v_pk_fma_f32 v[62:63], v[62:63], v[238:239], v[236:237] op_sel_hi:[1,0,1]
	v_exp_f32_e32 v130, v130
	v_exp_f32_e32 v131, v131
	v_exp_f32_e32 v132, v132
	v_exp_f32_e32 v133, v133
	v_exp_f32_e32 v60, v60
	v_exp_f32_e32 v61, v61
	v_exp_f32_e32 v62, v62
	v_exp_f32_e32 v63, v63
	v_pk_fma_f32 v[130:131], v[130:131], v[156:157], v[156:157] op_sel_hi:[1,0,0]
	v_pk_fma_f32 v[132:133], v[132:133], v[156:157], v[156:157] op_sel_hi:[1,0,0]
	v_pk_fma_f32 v[60:61], v[60:61], v[156:157], v[156:157] op_sel_hi:[1,0,0]
	v_pk_fma_f32 v[62:63], v[62:63], v[156:157], v[156:157] op_sel_hi:[1,0,0]
	v_rcp_f32_e32 v130, v130
	v_rcp_f32_e32 v131, v131
	v_rcp_f32_e32 v132, v132
	v_rcp_f32_e32 v133, v133
	v_rcp_f32_e32 v60, v60
	v_rcp_f32_e32 v61, v61
	v_rcp_f32_e32 v62, v62
	v_rcp_f32_e32 v63, v63
	s_nop 0
	v_rndne_f32_e32 v130, v130
	v_rndne_f32_e32 v131, v131
	v_rndne_f32_e32 v132, v132
	v_rndne_f32_e32 v133, v133
	v_rndne_f32_e32 v60, v60
	v_rndne_f32_e32 v61, v61
	v_rndne_f32_e32 v62, v62
	v_rndne_f32_e32 v63, v63
	v_max_f32_e32 v130, 1.0, v130
	v_max_f32_e32 v131, 1.0, v131
	v_max_f32_e32 v132, 1.0, v132
	v_max_f32_e32 v133, 1.0, v133
	v_max_f32_e32 v60, 1.0, v60
	v_max_f32_e32 v61, 1.0, v61
	v_max_f32_e32 v62, 1.0, v62
	v_max_f32_e32 v63, 1.0, v63
	v_cvt_pk_u8_f32 v146, v130, 0, 0
	v_cvt_pk_u8_f32 v147, v60, 0, 0
	v_cvt_pk_u8_f32 v146, v131, 1, v146
	v_cvt_pk_u8_f32 v147, v61, 1, v147
; __device__ __forceinline__ float sigmoidf_fast(float x) { return fast_rcp(1.0f + fast_exp2(-x * LOG2E)); }
; #define ROW_FENCE() asm volatile("" ::: "memory")
;     __device__ __forceinline__ void operator()(const pg8::i32x4 (&acc)[2][2][4][2], const pg8::Unit& u, int wr, int wc, int fr, int fq) const {
;     ...
;         for (int ai = 0; ai < 2; ++ai)
; #pragma unroll
;             for (int m = 0; m < 4; ++m) {
;                 const int row = u.pm * 256 + ai * 128 + wr * 64 + m * 16 + fr; const float r = rsv[ai][m];
;                 u32x4 gq = {0u, 0u, 0u, 0u};
; #pragma unroll
;                 for (int bj = 0; bj < 2; ++bj)
; #pragma unroll
;                     for (int n = 0; n < 2; ++n)
; #pragma unroll
;                         for (int j = 0; j < 4; ++j) gq[2 * bj + n] = __builtin_amdgcn_cvt_pk_u8_f32(fmaxf(__builtin_rintf(sigmoidf_fast((float)acc[ai][bj][m][n][j] * (r * cs[bj][n][j]) + bg[bj][n][j]) * 255.0f), 1.0f), j, gq[2 * bj + n]);
;                 if (!dry) *(u32x4*)(G + (ai * 4 + m) * 8192) = gq;
;                 ROW_FENCE();
	v_cvt_pk_u8_f32 v146, v132, 2, v146
	v_cvt_pk_u8_f32 v147, v62, 2, v147
	v_cvt_pk_u8_f32 v146, v133, 3, v146
	v_cvt_pk_u8_f32 v147, v63, 3, v147
	s_nop 0
	global_store_dwordx4 v153, v[144:147], s[22:23]
	v_cvt_f32_i32_e32 v122, v122
	v_cvt_f32_i32_e32 v123, v123
	v_cvt_f32_i32_e32 v124, v124
	v_cvt_f32_i32_e32 v125, v125
	v_cvt_f32_i32_e32 v118, v118
	v_cvt_f32_i32_e32 v119, v119
	v_cvt_f32_i32_e32 v120, v120
	v_cvt_f32_i32_e32 v121, v121
	v_pk_mul_f32 v[122:123], v[122:123], v[206:207]
	v_pk_mul_f32 v[124:125], v[124:125], v[208:209]
	v_pk_mul_f32 v[118:119], v[118:119], v[210:211]
	v_pk_mul_f32 v[120:121], v[120:121], v[212:213]
	v_pk_fma_f32 v[122:123], v[122:123], v[238:239], v[222:223] op_sel:[0,1,0] op_sel_hi:[1,1,1]
	v_pk_fma_f32 v[124:125], v[124:125], v[238:239], v[224:225] op_sel:[0,1,0] op_sel_hi:[1,1,1]
	v_pk_fma_f32 v[118:119], v[118:119], v[238:239], v[226:227] op_sel:[0,1,0] op_sel_hi:[1,1,1]
	v_pk_fma_f32 v[120:121], v[120:121], v[238:239], v[228:229] op_sel:[0,1,0] op_sel_hi:[1,1,1]
	v_exp_f32_e32 v122, v122
	v_exp_f32_e32 v123, v123
	v_exp_f32_e32 v124, v124
	v_exp_f32_e32 v125, v125
	v_exp_f32_e32 v118, v118
	v_exp_f32_e32 v119, v119
	v_exp_f32_e32 v120, v120
	v_exp_f32_e32 v121, v121
	v_pk_fma_f32 v[122:123], v[122:123], v[156:157], v[156:157] op_sel_hi:[1,0,0]
	v_pk_fma_f32 v[124:125], v[124:125], v[156:157], v[156:157] op_sel_hi:[1,0,0]
	v_pk_fma_f32 v[118:119], v[118:119], v[156:157], v[156:157] op_sel_hi:[1,0,0]
	v_pk_fma_f32 v[120:121], v[120:121], v[156:157], v[156:157] op_sel_hi:[1,0,0]
	v_rcp_f32_e32 v122, v122
	v_rcp_f32_e32 v123, v123
	v_rcp_f32_e32 v124, v124
	v_rcp_f32_e32 v125, v125
	v_rcp_f32_e32 v118, v118
	v_rcp_f32_e32 v119, v119
	v_rcp_f32_e32 v120, v120
	v_rcp_f32_e32 v121, v121
	v_add_u32_e32 v153, 0x2000, v152
	v_rndne_f32_e32 v122, v122
	v_rndne_f32_e32 v123, v123
	v_rndne_f32_e32 v124, v124
	v_rndne_f32_e32 v125, v125
	v_rndne_f32_e32 v118, v118
	v_rndne_f32_e32 v119, v119
	v_rndne_f32_e32 v120, v120
	v_rndne_f32_e32 v121, v121
	v_max_f32_e32 v122, 1.0, v122
	v_max_f32_e32 v123, 1.0, v123
	v_max_f32_e32 v124, 1.0, v124
	v_max_f32_e32 v125, 1.0, v125
	v_max_f32_e32 v118, 1.0, v118
	v_max_f32_e32 v119, 1.0, v119
	v_max_f32_e32 v120, 1.0, v120
	v_max_f32_e32 v121, 1.0, v121
	v_cvt_pk_u8_f32 v148, v122, 0, 0
	v_cvt_pk_u8_f32 v149, v118, 0, 0
	v_cvt_pk_u8_f32 v148, v123, 1, v148
	v_cvt_pk_u8_f32 v149, v119, 1, v149
	v_cvt_pk_u8_f32 v148, v124, 2, v148
	v_cvt_pk_u8_f32 v149, v120, 2, v149
	v_cvt_pk_u8_f32 v148, v125, 3, v148
	v_cvt_pk_u8_f32 v149, v121, 3, v149
	v_cvt_f32_i32_e32 v114, v114
	v_cvt_f32_i32_e32 v115, v115
	v_cvt_f32_i32_e32 v116, v116
	v_cvt_f32_i32_e32 v117, v117
	v_cvt_f32_i32_e32 v126, v126
	v_cvt_f32_i32_e32 v127, v127
	v_cvt_f32_i32_e32 v128, v128
	v_cvt_f32_i32_e32 v129, v129
	v_pk_mul_f32 v[114:115], v[114:115], v[214:215]
	v_pk_mul_f32 v[116:117], v[116:117], v[216:217]
	v_pk_mul_f32 v[126:127], v[126:127], v[218:219]
	v_pk_mul_f32 v[128:129], v[128:129], v[220:221]
	v_pk_fma_f32 v[114:115], v[114:115], v[238:239], v[230:231] op_sel:[0,1,0] op_sel_hi:[1,1,1]
	v_pk_fma_f32 v[116:117], v[116:117], v[238:239], v[232:233] op_sel:[0,1,0] op_sel_hi:[1,1,1]
	v_pk_fma_f32 v[126:127], v[126:127], v[238:239], v[234:235] op_sel:[0,1,0] op_sel_hi:[1,1,1]
	v_pk_fma_f32 v[128:129], v[128:129], v[238:239], v[236:237] op_sel:[0,1,0] op_sel_hi:[1,1,1]
	v_exp_f32_e32 v114, v114
	v_exp_f32_e32 v115, v115
	v_exp_f32_e32 v116, v116
	v_exp_f32_e32 v117, v117
	v_exp_f32_e32 v126, v126
	v_exp_f32_e32 v127, v127
	v_exp_f32_e32 v128, v128
	v_exp_f32_e32 v129, v129
	v_pk_fma_f32 v[114:115], v[114:115], v[156:157], v[156:157] op_sel_hi:[1,0,0]
	v_pk_fma_f32 v[116:117], v[116:117], v[156:157], v[156:157] op_sel_hi:[1,0,0]
	v_pk_fma_f32 v[126:127], v[126:127], v[156:157], v[156:157] op_sel_hi:[1,0,0]
	v_pk_fma_f32 v[128:129], v[128:129], v[156:157], v[156:157] op_sel_hi:[1,0,0]
	v_rcp_f32_e32 v114, v114
	v_rcp_f32_e32 v115, v115
	v_rcp_f32_e32 v116, v116
	v_rcp_f32_e32 v117, v117
	v_rcp_f32_e32 v126, v126
	v_rcp_f32_e32 v127, v127
	v_rcp_f32_e32 v128, v128
	v_rcp_f32_e32 v129, v129
	s_nop 0
	v_rndne_f32_e32 v114, v114
	v_rndne_f32_e32 v115, v115
	v_rndne_f32_e32 v116, v116
	v_rndne_f32_e32 v117, v117
	v_rndne_f32_e32 v126, v126
	v_rndne_f32_e32 v127, v127
	v_rndne_f32_e32 v128, v128
	v_rndne_f32_e32 v129, v129
	v_max_f32_e32 v114, 1.0, v114
	v_max_f32_e32 v115, 1.0, v115
	v_max_f32_e32 v116, 1.0, v116
	v_max_f32_e32 v117, 1.0, v117
	v_max_f32_e32 v126, 1.0, v126
	v_max_f32_e32 v127, 1.0, v127
	v_max_f32_e32 v128, 1.0, v128
	v_max_f32_e32 v129, 1.0, v129
	v_cvt_pk_u8_f32 v150, v114, 0, 0
	v_cvt_pk_u8_f32 v151, v126, 0, 0
	v_cvt_pk_u8_f32 v150, v115, 1, v150
	v_cvt_pk_u8_f32 v151, v127, 1, v151
	v_cvt_pk_u8_f32 v150, v116, 2, v150
	v_cvt_pk_u8_f32 v151, v128, 2, v151
	v_cvt_pk_u8_f32 v150, v117, 3, v150
	v_cvt_pk_u8_f32 v151, v129, 3, v151
	s_nop 0
	global_store_dwordx4 v153, v[148:151], s[22:23]
	v_cvt_f32_i32_e32 v104, v104
	v_cvt_f32_i32_e32 v105, v105
	v_cvt_f32_i32_e32 v106, v106
	v_cvt_f32_i32_e32 v107, v107
	v_cvt_f32_i32_e32 v100, v100
	v_cvt_f32_i32_e32 v101, v101
	v_cvt_f32_i32_e32 v102, v102
	v_cvt_f32_i32_e32 v103, v103
	v_pk_mul_f32 v[104:105], v[104:105], v[206:207]
	v_pk_mul_f32 v[106:107], v[106:107], v[208:209]
	v_pk_mul_f32 v[100:101], v[100:101], v[210:211]
	v_pk_mul_f32 v[102:103], v[102:103], v[212:213]
	v_pk_fma_f32 v[104:105], v[104:105], v[240:241], v[222:223] op_sel_hi:[1,0,1]
	v_pk_fma_f32 v[106:107], v[106:107], v[240:241], v[224:225] op_sel_hi:[1,0,1]
	v_pk_fma_f32 v[100:101], v[100:101], v[240:241], v[226:227] op_sel_hi:[1,0,1]
	v_pk_fma_f32 v[102:103], v[102:103], v[240:241], v[228:229] op_sel_hi:[1,0,1]
; __device__ __forceinline__ float sigmoidf_fast(float x) { return fast_rcp(1.0f + fast_exp2(-x * LOG2E)); }
; #define ROW_FENCE() asm volatile("" ::: "memory")
;     __device__ __forceinline__ void operator()(const pg8::i32x4 (&acc)[2][2][4][2], const pg8::Unit& u, int wr, int wc, int fr, int fq) const {
;     ...
;         for (int ai = 0; ai < 2; ++ai)
; #pragma unroll
;             for (int m = 0; m < 4; ++m) {
;                 const int row = u.pm * 256 + ai * 128 + wr * 64 + m * 16 + fr; const float r = rsv[ai][m];
;                 u32x4 gq = {0u, 0u, 0u, 0u};
; #pragma unroll
;                 for (int bj = 0; bj < 2; ++bj)
; #pragma unroll
;                     for (int n = 0; n < 2; ++n)
; #pragma unroll
;                         for (int j = 0; j < 4; ++j) gq[2 * bj + n] = __builtin_amdgcn_cvt_pk_u8_f32(fmaxf(__builtin_rintf(sigmoidf_fast((float)acc[ai][bj][m][n][j] * (r * cs[bj][n][j]) + bg[bj][n][j]) * 255.0f), 1.0f), j, gq[2 * bj + n]);
;                 if (!dry) *(u32x4*)(G + (ai * 4 + m) * 8192) = gq;
;                 ROW_FENCE();
	v_exp_f32_e32 v104, v104
	v_exp_f32_e32 v105, v105
	v_exp_f32_e32 v106, v106
	v_exp_f32_e32 v107, v107
	v_exp_f32_e32 v100, v100
	v_exp_f32_e32 v101, v101
	v_exp_f32_e32 v102, v102
	v_exp_f32_e32 v103, v103
	v_pk_fma_f32 v[104:105], v[104:105], v[156:157], v[156:157] op_sel_hi:[1,0,0]
	v_pk_fma_f32 v[106:107], v[106:107], v[156:157], v[156:157] op_sel_hi:[1,0,0]
	v_pk_fma_f32 v[100:101], v[100:101], v[156:157], v[156:157] op_sel_hi:[1,0,0]
	v_pk_fma_f32 v[102:103], v[102:103], v[156:157], v[156:157] op_sel_hi:[1,0,0]
	v_rcp_f32_e32 v104, v104
	v_rcp_f32_e32 v105, v105
	v_rcp_f32_e32 v106, v106
	v_rcp_f32_e32 v107, v107
	v_rcp_f32_e32 v100, v100
	v_rcp_f32_e32 v101, v101
	v_rcp_f32_e32 v102, v102
	v_rcp_f32_e32 v103, v103
	v_add_u32_e32 v153, 0x4000, v152
	v_rndne_f32_e32 v104, v104
	v_rndne_f32_e32 v105, v105
	v_rndne_f32_e32 v106, v106
	v_rndne_f32_e32 v107, v107
	v_rndne_f32_e32 v100, v100
	v_rndne_f32_e32 v101, v101
	v_rndne_f32_e32 v102, v102
	v_rndne_f32_e32 v103, v103
	v_max_f32_e32 v104, 1.0, v104
	v_max_f32_e32 v105, 1.0, v105
	v_max_f32_e32 v106, 1.0, v106
	v_max_f32_e32 v107, 1.0, v107
	v_max_f32_e32 v100, 1.0, v100
	v_max_f32_e32 v101, 1.0, v101
	v_max_f32_e32 v102, 1.0, v102
	v_max_f32_e32 v103, 1.0, v103
	v_cvt_pk_u8_f32 v144, v104, 0, 0
	v_cvt_pk_u8_f32 v145, v100, 0, 0
	v_cvt_pk_u8_f32 v144, v105, 1, v144
	v_cvt_pk_u8_f32 v145, v101, 1, v145
	v_cvt_pk_u8_f32 v144, v106, 2, v144
	v_cvt_pk_u8_f32 v145, v102, 2, v145
	v_cvt_pk_u8_f32 v144, v107, 3, v144
	v_cvt_pk_u8_f32 v145, v103, 3, v145
	v_cvt_f32_i32_e32 v96, v96
	v_cvt_f32_i32_e32 v97, v97
	v_cvt_f32_i32_e32 v98, v98
	v_cvt_f32_i32_e32 v99, v99
	v_cvt_f32_i32_e32 v108, v108
	v_cvt_f32_i32_e32 v109, v109
	v_cvt_f32_i32_e32 v110, v110
	v_cvt_f32_i32_e32 v111, v111
	v_pk_mul_f32 v[96:97], v[96:97], v[214:215]
	v_pk_mul_f32 v[98:99], v[98:99], v[216:217]
	v_pk_mul_f32 v[108:109], v[108:109], v[218:219]
	v_pk_mul_f32 v[110:111], v[110:111], v[220:221]
	v_pk_fma_f32 v[96:97], v[96:97], v[240:241], v[230:231] op_sel_hi:[1,0,1]
	v_pk_fma_f32 v[98:99], v[98:99], v[240:241], v[232:233] op_sel_hi:[1,0,1]
	v_pk_fma_f32 v[108:109], v[108:109], v[240:241], v[234:235] op_sel_hi:[1,0,1]
	v_pk_fma_f32 v[110:111], v[110:111], v[240:241], v[236:237] op_sel_hi:[1,0,1]
	v_exp_f32_e32 v96, v96
	v_exp_f32_e32 v97, v97
	v_exp_f32_e32 v98, v98
	v_exp_f32_e32 v99, v99
	v_exp_f32_e32 v108, v108
	v_exp_f32_e32 v109, v109
	v_exp_f32_e32 v110, v110
	v_exp_f32_e32 v111, v111
	v_pk_fma_f32 v[96:97], v[96:97], v[156:157], v[156:157] op_sel_hi:[1,0,0]
	v_pk_fma_f32 v[98:99], v[98:99], v[156:157], v[156:157] op_sel_hi:[1,0,0]
	v_pk_fma_f32 v[108:109], v[108:109], v[156:157], v[156:157] op_sel_hi:[1,0,0]
	v_pk_fma_f32 v[110:111], v[110:111], v[156:157], v[156:157] op_sel_hi:[1,0,0]
	v_rcp_f32_e32 v96, v96
	v_rcp_f32_e32 v97, v97
	v_rcp_f32_e32 v98, v98
	v_rcp_f32_e32 v99, v99
	v_rcp_f32_e32 v108, v108
	v_rcp_f32_e32 v109, v109
	v_rcp_f32_e32 v110, v110
	v_rcp_f32_e32 v111, v111
	s_nop 0
	v_rndne_f32_e32 v96, v96
	v_rndne_f32_e32 v97, v97
	v_rndne_f32_e32 v98, v98
	v_rndne_f32_e32 v99, v99
	v_rndne_f32_e32 v108, v108
	v_rndne_f32_e32 v109, v109
	v_rndne_f32_e32 v110, v110
	v_rndne_f32_e32 v111, v111
	v_max_f32_e32 v96, 1.0, v96
	v_max_f32_e32 v97, 1.0, v97
	v_max_f32_e32 v98, 1.0, v98
	v_max_f32_e32 v99, 1.0, v99
	v_max_f32_e32 v108, 1.0, v108
	v_max_f32_e32 v109, 1.0, v109
	v_max_f32_e32 v110, 1.0, v110
	v_max_f32_e32 v111, 1.0, v111
	v_cvt_pk_u8_f32 v146, v96, 0, 0
	v_cvt_pk_u8_f32 v147, v108, 0, 0
	v_cvt_pk_u8_f32 v146, v97, 1, v146
	v_cvt_pk_u8_f32 v147, v109, 1, v147
	v_cvt_pk_u8_f32 v146, v98, 2, v146
	v_cvt_pk_u8_f32 v147, v110, 2, v147
	v_cvt_pk_u8_f32 v146, v99, 3, v146
	v_cvt_pk_u8_f32 v147, v111, 3, v147
	s_nop 0
	global_store_dwordx4 v153, v[144:147], s[22:23]
	v_cvt_f32_i32_e32 v88, v88
	v_cvt_f32_i32_e32 v89, v89
	v_cvt_f32_i32_e32 v90, v90
	v_cvt_f32_i32_e32 v91, v91
	v_cvt_f32_i32_e32 v84, v84
	v_cvt_f32_i32_e32 v85, v85
	v_cvt_f32_i32_e32 v86, v86
	v_cvt_f32_i32_e32 v87, v87
	v_pk_mul_f32 v[88:89], v[88:89], v[206:207]
	v_pk_mul_f32 v[90:91], v[90:91], v[208:209]
	v_pk_mul_f32 v[84:85], v[84:85], v[210:211]
	v_pk_mul_f32 v[86:87], v[86:87], v[212:213]
	v_pk_fma_f32 v[88:89], v[88:89], v[240:241], v[222:223] op_sel:[0,1,0] op_sel_hi:[1,1,1]
	v_pk_fma_f32 v[90:91], v[90:91], v[240:241], v[224:225] op_sel:[0,1,0] op_sel_hi:[1,1,1]
	v_pk_fma_f32 v[84:85], v[84:85], v[240:241], v[226:227] op_sel:[0,1,0] op_sel_hi:[1,1,1]
	v_pk_fma_f32 v[86:87], v[86:87], v[240:241], v[228:229] op_sel:[0,1,0] op_sel_hi:[1,1,1]
	v_exp_f32_e32 v88, v88
	v_exp_f32_e32 v89, v89
	v_exp_f32_e32 v90, v90
	v_exp_f32_e32 v91, v91
	v_exp_f32_e32 v84, v84
	v_exp_f32_e32 v85, v85
	v_exp_f32_e32 v86, v86
	v_exp_f32_e32 v87, v87
	v_pk_fma_f32 v[88:89], v[88:89], v[156:157], v[156:157] op_sel_hi:[1,0,0]
	v_pk_fma_f32 v[90:91], v[90:91], v[156:157], v[156:157] op_sel_hi:[1,0,0]
	v_pk_fma_f32 v[84:85], v[84:85], v[156:157], v[156:157] op_sel_hi:[1,0,0]
	v_pk_fma_f32 v[86:87], v[86:87], v[156:157], v[156:157] op_sel_hi:[1,0,0]
	v_rcp_f32_e32 v88, v88
	v_rcp_f32_e32 v89, v89
	v_rcp_f32_e32 v90, v90
	v_rcp_f32_e32 v91, v91
	v_rcp_f32_e32 v84, v84
	v_rcp_f32_e32 v85, v85
	v_rcp_f32_e32 v86, v86
	v_rcp_f32_e32 v87, v87
	v_add_u32_e32 v153, 0x6000, v152
	v_rndne_f32_e32 v88, v88
	v_rndne_f32_e32 v89, v89
	v_rndne_f32_e32 v90, v90
	v_rndne_f32_e32 v91, v91
	v_rndne_f32_e32 v84, v84
	v_rndne_f32_e32 v85, v85
	v_rndne_f32_e32 v86, v86
	v_rndne_f32_e32 v87, v87
	v_max_f32_e32 v88, 1.0, v88
	v_max_f32_e32 v89, 1.0, v89
	v_max_f32_e32 v90, 1.0, v90
	v_max_f32_e32 v91, 1.0, v91
	v_max_f32_e32 v84, 1.0, v84
	v_max_f32_e32 v85, 1.0, v85
; __device__ __forceinline__ float sigmoidf_fast(float x) { return fast_rcp(1.0f + fast_exp2(-x * LOG2E)); }
; #define ROW_FENCE() asm volatile("" ::: "memory")
;     __device__ __forceinline__ void operator()(const pg8::i32x4 (&acc)[2][2][4][2], const pg8::Unit& u, int wr, int wc, int fr, int fq) const {
;     ...
;         for (int ai = 0; ai < 2; ++ai)
; #pragma unroll
;             for (int m = 0; m < 4; ++m) {
;                 const int row = u.pm * 256 + ai * 128 + wr * 64 + m * 16 + fr; const float r = rsv[ai][m];
;                 u32x4 gq = {0u, 0u, 0u, 0u};
; #pragma unroll
;                 for (int bj = 0; bj < 2; ++bj)
; #pragma unroll
;                     for (int n = 0; n < 2; ++n)
; #pragma unroll
;                         for (int j = 0; j < 4; ++j) gq[2 * bj + n] = __builtin_amdgcn_cvt_pk_u8_f32(fmaxf(__builtin_rintf(sigmoidf_fast((float)acc[ai][bj][m][n][j] * (r * cs[bj][n][j]) + bg[bj][n][j]) * 255.0f), 1.0f), j, gq[2 * bj + n]);
;                 if (!dry) *(u32x4*)(G + (ai * 4 + m) * 8192) = gq;
;                 ROW_FENCE();
	v_max_f32_e32 v86, 1.0, v86
	v_max_f32_e32 v87, 1.0, v87
	v_cvt_pk_u8_f32 v148, v88, 0, 0
	v_cvt_pk_u8_f32 v149, v84, 0, 0
	v_cvt_pk_u8_f32 v148, v89, 1, v148
	v_cvt_pk_u8_f32 v149, v85, 1, v149
	v_cvt_pk_u8_f32 v148, v90, 2, v148
	v_cvt_pk_u8_f32 v149, v86, 2, v149
	v_cvt_pk_u8_f32 v148, v91, 3, v148
	v_cvt_pk_u8_f32 v149, v87, 3, v149
	v_cvt_f32_i32_e32 v80, v80
	v_cvt_f32_i32_e32 v81, v81
	v_cvt_f32_i32_e32 v82, v82
	v_cvt_f32_i32_e32 v83, v83
	v_cvt_f32_i32_e32 v92, v92
	v_cvt_f32_i32_e32 v93, v93
	v_cvt_f32_i32_e32 v94, v94
	v_cvt_f32_i32_e32 v95, v95
	v_pk_mul_f32 v[80:81], v[80:81], v[214:215]
	v_pk_mul_f32 v[82:83], v[82:83], v[216:217]
	v_pk_mul_f32 v[92:93], v[92:93], v[218:219]
	v_pk_mul_f32 v[94:95], v[94:95], v[220:221]
	v_pk_fma_f32 v[80:81], v[80:81], v[240:241], v[230:231] op_sel:[0,1,0] op_sel_hi:[1,1,1]
	v_pk_fma_f32 v[82:83], v[82:83], v[240:241], v[232:233] op_sel:[0,1,0] op_sel_hi:[1,1,1]
	v_pk_fma_f32 v[92:93], v[92:93], v[240:241], v[234:235] op_sel:[0,1,0] op_sel_hi:[1,1,1]
	v_pk_fma_f32 v[94:95], v[94:95], v[240:241], v[236:237] op_sel:[0,1,0] op_sel_hi:[1,1,1]
	v_exp_f32_e32 v80, v80
	v_exp_f32_e32 v81, v81
	v_exp_f32_e32 v82, v82
	v_exp_f32_e32 v83, v83
	v_exp_f32_e32 v92, v92
	v_exp_f32_e32 v93, v93
	v_exp_f32_e32 v94, v94
	v_exp_f32_e32 v95, v95
	v_pk_fma_f32 v[80:81], v[80:81], v[156:157], v[156:157] op_sel_hi:[1,0,0]
	v_pk_fma_f32 v[82:83], v[82:83], v[156:157], v[156:157] op_sel_hi:[1,0,0]
	v_pk_fma_f32 v[92:93], v[92:93], v[156:157], v[156:157] op_sel_hi:[1,0,0]
	v_pk_fma_f32 v[94:95], v[94:95], v[156:157], v[156:157] op_sel_hi:[1,0,0]
	v_rcp_f32_e32 v80, v80
	v_rcp_f32_e32 v81, v81
	v_rcp_f32_e32 v82, v82
	v_rcp_f32_e32 v83, v83
	v_rcp_f32_e32 v92, v92
	v_rcp_f32_e32 v93, v93
	v_rcp_f32_e32 v94, v94
	v_rcp_f32_e32 v95, v95
	s_nop 0
	v_rndne_f32_e32 v80, v80
	v_rndne_f32_e32 v81, v81
	v_rndne_f32_e32 v82, v82
	v_rndne_f32_e32 v83, v83
	v_rndne_f32_e32 v92, v92
	v_rndne_f32_e32 v93, v93
	v_rndne_f32_e32 v94, v94
	v_rndne_f32_e32 v95, v95
	v_max_f32_e32 v80, 1.0, v80
	v_max_f32_e32 v81, 1.0, v81
	v_max_f32_e32 v82, 1.0, v82
	v_max_f32_e32 v83, 1.0, v83
	v_max_f32_e32 v92, 1.0, v92
	v_max_f32_e32 v93, 1.0, v93
	v_max_f32_e32 v94, 1.0, v94
	v_max_f32_e32 v95, 1.0, v95
	v_cvt_pk_u8_f32 v150, v80, 0, 0
	v_cvt_pk_u8_f32 v151, v92, 0, 0
	v_cvt_pk_u8_f32 v150, v81, 1, v150
	v_cvt_pk_u8_f32 v151, v93, 1, v151
	v_cvt_pk_u8_f32 v150, v82, 2, v150
	v_cvt_pk_u8_f32 v151, v94, 2, v151
	v_cvt_pk_u8_f32 v150, v83, 3, v150
	v_cvt_pk_u8_f32 v151, v95, 3, v151
	s_nop 0
	global_store_dwordx4 v153, v[148:151], s[22:23]
	v_cvt_f32_i32_e32 v56, v56
	v_cvt_f32_i32_e32 v57, v57
	v_cvt_f32_i32_e32 v58, v58
	v_cvt_f32_i32_e32 v59, v59
	v_cvt_f32_i32_e32 v52, v52
	v_cvt_f32_i32_e32 v53, v53
	v_cvt_f32_i32_e32 v54, v54
	v_cvt_f32_i32_e32 v55, v55
	v_pk_mul_f32 v[56:57], v[56:57], v[206:207]
	v_pk_mul_f32 v[58:59], v[58:59], v[208:209]
	v_pk_mul_f32 v[52:53], v[52:53], v[210:211]
	v_pk_mul_f32 v[54:55], v[54:55], v[212:213]
	v_pk_fma_f32 v[56:57], v[56:57], v[242:243], v[222:223] op_sel_hi:[1,0,1]
	v_pk_fma_f32 v[58:59], v[58:59], v[242:243], v[224:225] op_sel_hi:[1,0,1]
	v_pk_fma_f32 v[52:53], v[52:53], v[242:243], v[226:227] op_sel_hi:[1,0,1]
	v_pk_fma_f32 v[54:55], v[54:55], v[242:243], v[228:229] op_sel_hi:[1,0,1]
	v_exp_f32_e32 v56, v56
	v_exp_f32_e32 v57, v57
	v_exp_f32_e32 v58, v58
	v_exp_f32_e32 v59, v59
	v_exp_f32_e32 v52, v52
	v_exp_f32_e32 v53, v53
	v_exp_f32_e32 v54, v54
	v_exp_f32_e32 v55, v55
	v_pk_fma_f32 v[56:57], v[56:57], v[156:157], v[156:157] op_sel_hi:[1,0,0]
	v_pk_fma_f32 v[58:59], v[58:59], v[156:157], v[156:157] op_sel_hi:[1,0,0]
	v_pk_fma_f32 v[52:53], v[52:53], v[156:157], v[156:157] op_sel_hi:[1,0,0]
	v_pk_fma_f32 v[54:55], v[54:55], v[156:157], v[156:157] op_sel_hi:[1,0,0]
	v_rcp_f32_e32 v56, v56
	v_rcp_f32_e32 v57, v57
	v_rcp_f32_e32 v58, v58
	v_rcp_f32_e32 v59, v59
	v_rcp_f32_e32 v52, v52
	v_rcp_f32_e32 v53, v53
	v_rcp_f32_e32 v54, v54
	v_rcp_f32_e32 v55, v55
	v_add_u32_e32 v153, 0x8000, v152
	v_rndne_f32_e32 v56, v56
	v_rndne_f32_e32 v57, v57
	v_rndne_f32_e32 v58, v58
	v_rndne_f32_e32 v59, v59
	v_rndne_f32_e32 v52, v52
	v_rndne_f32_e32 v53, v53
	v_rndne_f32_e32 v54, v54
	v_rndne_f32_e32 v55, v55
	v_max_f32_e32 v56, 1.0, v56
	v_max_f32_e32 v57, 1.0, v57
	v_max_f32_e32 v58, 1.0, v58
	v_max_f32_e32 v59, 1.0, v59
	v_max_f32_e32 v52, 1.0, v52
	v_max_f32_e32 v53, 1.0, v53
	v_max_f32_e32 v54, 1.0, v54
	v_max_f32_e32 v55, 1.0, v55
	v_cvt_pk_u8_f32 v144, v56, 0, 0
	v_cvt_pk_u8_f32 v145, v52, 0, 0
	v_cvt_pk_u8_f32 v144, v57, 1, v144
	v_cvt_pk_u8_f32 v145, v53, 1, v145
	v_cvt_pk_u8_f32 v144, v58, 2, v144
	v_cvt_pk_u8_f32 v145, v54, 2, v145
	v_cvt_pk_u8_f32 v144, v59, 3, v144
	v_cvt_pk_u8_f32 v145, v55, 3, v145
	v_cvt_f32_i32_e32 v48, v48
	v_cvt_f32_i32_e32 v49, v49
	v_cvt_f32_i32_e32 v50, v50
	v_cvt_f32_i32_e32 v51, v51
	v_cvt_f32_i32_e32 v64, v64
	v_cvt_f32_i32_e32 v65, v65
	v_cvt_f32_i32_e32 v66, v66
	v_cvt_f32_i32_e32 v67, v67
	v_pk_mul_f32 v[48:49], v[48:49], v[214:215]
	v_pk_mul_f32 v[50:51], v[50:51], v[216:217]
	v_pk_mul_f32 v[64:65], v[64:65], v[218:219]
	v_pk_mul_f32 v[66:67], v[66:67], v[220:221]
	v_pk_fma_f32 v[48:49], v[48:49], v[242:243], v[230:231] op_sel_hi:[1,0,1]
	v_pk_fma_f32 v[50:51], v[50:51], v[242:243], v[232:233] op_sel_hi:[1,0,1]
	v_pk_fma_f32 v[64:65], v[64:65], v[242:243], v[234:235] op_sel_hi:[1,0,1]
	v_pk_fma_f32 v[66:67], v[66:67], v[242:243], v[236:237] op_sel_hi:[1,0,1]
	v_exp_f32_e32 v48, v48
	v_exp_f32_e32 v49, v49
	v_exp_f32_e32 v50, v50
	v_exp_f32_e32 v51, v51
	v_exp_f32_e32 v64, v64
	v_exp_f32_e32 v65, v65
	v_exp_f32_e32 v66, v66
	v_exp_f32_e32 v67, v67
; __device__ __forceinline__ float sigmoidf_fast(float x) { return fast_rcp(1.0f + fast_exp2(-x * LOG2E)); }
; #define ROW_FENCE() asm volatile("" ::: "memory")
;     __device__ __forceinline__ void operator()(const pg8::i32x4 (&acc)[2][2][4][2], const pg8::Unit& u, int wr, int wc, int fr, int fq) const {
;     ...
;         for (int ai = 0; ai < 2; ++ai)
; #pragma unroll
;             for (int m = 0; m < 4; ++m) {
;                 const int row = u.pm * 256 + ai * 128 + wr * 64 + m * 16 + fr; const float r = rsv[ai][m];
;                 u32x4 gq = {0u, 0u, 0u, 0u};
; #pragma unroll
;                 for (int bj = 0; bj < 2; ++bj)
; #pragma unroll
;                     for (int n = 0; n < 2; ++n)
; #pragma unroll
;                         for (int j = 0; j < 4; ++j) gq[2 * bj + n] = __builtin_amdgcn_cvt_pk_u8_f32(fmaxf(__builtin_rintf(sigmoidf_fast((float)acc[ai][bj][m][n][j] * (r * cs[bj][n][j]) + bg[bj][n][j]) * 255.0f), 1.0f), j, gq[2 * bj + n]);
;                 if (!dry) *(u32x4*)(G + (ai * 4 + m) * 8192) = gq;
;                 ROW_FENCE();
	v_pk_fma_f32 v[48:49], v[48:49], v[156:157], v[156:157] op_sel_hi:[1,0,0]
	v_pk_fma_f32 v[50:51], v[50:51], v[156:157], v[156:157] op_sel_hi:[1,0,0]
	v_pk_fma_f32 v[64:65], v[64:65], v[156:157], v[156:157] op_sel_hi:[1,0,0]
	v_pk_fma_f32 v[66:67], v[66:67], v[156:157], v[156:157] op_sel_hi:[1,0,0]
	v_rcp_f32_e32 v48, v48
	v_rcp_f32_e32 v49, v49
	v_rcp_f32_e32 v50, v50
	v_rcp_f32_e32 v51, v51
	v_rcp_f32_e32 v64, v64
	v_rcp_f32_e32 v65, v65
	v_rcp_f32_e32 v66, v66
	v_rcp_f32_e32 v67, v67
	s_nop 0
	v_rndne_f32_e32 v48, v48
	v_rndne_f32_e32 v49, v49
	v_rndne_f32_e32 v50, v50
	v_rndne_f32_e32 v51, v51
	v_rndne_f32_e32 v64, v64
	v_rndne_f32_e32 v65, v65
	v_rndne_f32_e32 v66, v66
	v_rndne_f32_e32 v67, v67
	v_max_f32_e32 v48, 1.0, v48
	v_max_f32_e32 v49, 1.0, v49
	v_max_f32_e32 v50, 1.0, v50
	v_max_f32_e32 v51, 1.0, v51
	v_max_f32_e32 v64, 1.0, v64
	v_max_f32_e32 v65, 1.0, v65
	v_max_f32_e32 v66, 1.0, v66
	v_max_f32_e32 v67, 1.0, v67
	v_cvt_pk_u8_f32 v146, v48, 0, 0
	v_cvt_pk_u8_f32 v147, v64, 0, 0
	v_cvt_pk_u8_f32 v146, v49, 1, v146
	v_cvt_pk_u8_f32 v147, v65, 1, v147
	v_cvt_pk_u8_f32 v146, v50, 2, v146
	v_cvt_pk_u8_f32 v147, v66, 2, v147
	v_cvt_pk_u8_f32 v146, v51, 3, v146
	v_cvt_pk_u8_f32 v147, v67, 3, v147
	s_nop 0
	global_store_dwordx4 v153, v[144:147], s[22:23]
	v_cvt_f32_i32_e32 v40, v40
	v_cvt_f32_i32_e32 v41, v41
	v_cvt_f32_i32_e32 v42, v42
	v_cvt_f32_i32_e32 v43, v43
	v_cvt_f32_i32_e32 v36, v36
	v_cvt_f32_i32_e32 v37, v37
	v_cvt_f32_i32_e32 v38, v38
	v_cvt_f32_i32_e32 v39, v39
	v_pk_mul_f32 v[40:41], v[40:41], v[206:207]
	v_pk_mul_f32 v[42:43], v[42:43], v[208:209]
	v_pk_mul_f32 v[36:37], v[36:37], v[210:211]
	v_pk_mul_f32 v[38:39], v[38:39], v[212:213]
	v_pk_fma_f32 v[40:41], v[40:41], v[242:243], v[222:223] op_sel:[0,1,0] op_sel_hi:[1,1,1]
	v_pk_fma_f32 v[42:43], v[42:43], v[242:243], v[224:225] op_sel:[0,1,0] op_sel_hi:[1,1,1]
	v_pk_fma_f32 v[36:37], v[36:37], v[242:243], v[226:227] op_sel:[0,1,0] op_sel_hi:[1,1,1]
	v_pk_fma_f32 v[38:39], v[38:39], v[242:243], v[228:229] op_sel:[0,1,0] op_sel_hi:[1,1,1]
	v_exp_f32_e32 v40, v40
	v_exp_f32_e32 v41, v41
	v_exp_f32_e32 v42, v42
	v_exp_f32_e32 v43, v43
	v_exp_f32_e32 v36, v36
	v_exp_f32_e32 v37, v37
	v_exp_f32_e32 v38, v38
	v_exp_f32_e32 v39, v39
	v_pk_fma_f32 v[40:41], v[40:41], v[156:157], v[156:157] op_sel_hi:[1,0,0]
	v_pk_fma_f32 v[42:43], v[42:43], v[156:157], v[156:157] op_sel_hi:[1,0,0]
	v_pk_fma_f32 v[36:37], v[36:37], v[156:157], v[156:157] op_sel_hi:[1,0,0]
	v_pk_fma_f32 v[38:39], v[38:39], v[156:157], v[156:157] op_sel_hi:[1,0,0]
	v_rcp_f32_e32 v40, v40
	v_rcp_f32_e32 v41, v41
	v_rcp_f32_e32 v42, v42
	v_rcp_f32_e32 v43, v43
	v_rcp_f32_e32 v36, v36
	v_rcp_f32_e32 v37, v37
	v_rcp_f32_e32 v38, v38
	v_rcp_f32_e32 v39, v39
	v_add_u32_e32 v153, 0xa000, v152
	v_rndne_f32_e32 v40, v40
	v_rndne_f32_e32 v41, v41
	v_rndne_f32_e32 v42, v42
	v_rndne_f32_e32 v43, v43
	v_rndne_f32_e32 v36, v36
	v_rndne_f32_e32 v37, v37
	v_rndne_f32_e32 v38, v38
	v_rndne_f32_e32 v39, v39
	v_max_f32_e32 v40, 1.0, v40
	v_max_f32_e32 v41, 1.0, v41
	v_max_f32_e32 v42, 1.0, v42
	v_max_f32_e32 v43, 1.0, v43
	v_max_f32_e32 v36, 1.0, v36
	v_max_f32_e32 v37, 1.0, v37
	v_max_f32_e32 v38, 1.0, v38
	v_max_f32_e32 v39, 1.0, v39
	v_cvt_pk_u8_f32 v148, v40, 0, 0
	v_cvt_pk_u8_f32 v149, v36, 0, 0
	v_cvt_pk_u8_f32 v148, v41, 1, v148
	v_cvt_pk_u8_f32 v149, v37, 1, v149
	v_cvt_pk_u8_f32 v148, v42, 2, v148
	v_cvt_pk_u8_f32 v149, v38, 2, v149
	v_cvt_pk_u8_f32 v148, v43, 3, v148
	v_cvt_pk_u8_f32 v149, v39, 3, v149
	v_cvt_f32_i32_e32 v32, v32
	v_cvt_f32_i32_e32 v33, v33
	v_cvt_f32_i32_e32 v34, v34
	v_cvt_f32_i32_e32 v35, v35
	v_cvt_f32_i32_e32 v44, v44
	v_cvt_f32_i32_e32 v45, v45
	v_cvt_f32_i32_e32 v46, v46
	v_cvt_f32_i32_e32 v47, v47
	v_pk_mul_f32 v[32:33], v[32:33], v[214:215]
	v_pk_mul_f32 v[34:35], v[34:35], v[216:217]
	v_pk_mul_f32 v[44:45], v[44:45], v[218:219]
	v_pk_mul_f32 v[46:47], v[46:47], v[220:221]
	v_pk_fma_f32 v[32:33], v[32:33], v[242:243], v[230:231] op_sel:[0,1,0] op_sel_hi:[1,1,1]
	v_pk_fma_f32 v[34:35], v[34:35], v[242:243], v[232:233] op_sel:[0,1,0] op_sel_hi:[1,1,1]
	v_pk_fma_f32 v[44:45], v[44:45], v[242:243], v[234:235] op_sel:[0,1,0] op_sel_hi:[1,1,1]
	v_pk_fma_f32 v[46:47], v[46:47], v[242:243], v[236:237] op_sel:[0,1,0] op_sel_hi:[1,1,1]
	v_exp_f32_e32 v32, v32
	v_exp_f32_e32 v33, v33
	v_exp_f32_e32 v34, v34
	v_exp_f32_e32 v35, v35
	v_exp_f32_e32 v44, v44
	v_exp_f32_e32 v45, v45
	v_exp_f32_e32 v46, v46
	v_exp_f32_e32 v47, v47
	v_pk_fma_f32 v[32:33], v[32:33], v[156:157], v[156:157] op_sel_hi:[1,0,0]
	v_pk_fma_f32 v[34:35], v[34:35], v[156:157], v[156:157] op_sel_hi:[1,0,0]
	v_pk_fma_f32 v[44:45], v[44:45], v[156:157], v[156:157] op_sel_hi:[1,0,0]
	v_pk_fma_f32 v[46:47], v[46:47], v[156:157], v[156:157] op_sel_hi:[1,0,0]
	v_rcp_f32_e32 v32, v32
	v_rcp_f32_e32 v33, v33
	v_rcp_f32_e32 v34, v34
	v_rcp_f32_e32 v35, v35
	v_rcp_f32_e32 v44, v44
	v_rcp_f32_e32 v45, v45
	v_rcp_f32_e32 v46, v46
	v_rcp_f32_e32 v47, v47
	s_nop 0
	v_rndne_f32_e32 v32, v32
	v_rndne_f32_e32 v33, v33
	v_rndne_f32_e32 v34, v34
	v_rndne_f32_e32 v35, v35
	v_rndne_f32_e32 v44, v44
	v_rndne_f32_e32 v45, v45
	v_rndne_f32_e32 v46, v46
	v_rndne_f32_e32 v47, v47
	v_max_f32_e32 v32, 1.0, v32
	v_max_f32_e32 v33, 1.0, v33
	v_max_f32_e32 v34, 1.0, v34
	v_max_f32_e32 v35, 1.0, v35
	v_max_f32_e32 v44, 1.0, v44
	v_max_f32_e32 v45, 1.0, v45
	v_max_f32_e32 v46, 1.0, v46
	v_max_f32_e32 v47, 1.0, v47
	v_cvt_pk_u8_f32 v150, v32, 0, 0
	v_cvt_pk_u8_f32 v151, v44, 0, 0
	v_cvt_pk_u8_f32 v150, v33, 1, v150
	v_cvt_pk_u8_f32 v151, v45, 1, v151
	v_cvt_pk_u8_f32 v150, v34, 2, v150
	v_cvt_pk_u8_f32 v151, v46, 2, v151
	v_cvt_pk_u8_f32 v150, v35, 3, v150
; __device__ __forceinline__ float sigmoidf_fast(float x) { return fast_rcp(1.0f + fast_exp2(-x * LOG2E)); }
; #define ROW_FENCE() asm volatile("" ::: "memory")
;     __device__ __forceinline__ void operator()(const pg8::i32x4 (&acc)[2][2][4][2], const pg8::Unit& u, int wr, int wc, int fr, int fq) const {
;     ...
;         for (int ai = 0; ai < 2; ++ai)
; #pragma unroll
;             for (int m = 0; m < 4; ++m) {
;                 const int row = u.pm * 256 + ai * 128 + wr * 64 + m * 16 + fr; const float r = rsv[ai][m];
;                 u32x4 gq = {0u, 0u, 0u, 0u};
; #pragma unroll
;                 for (int bj = 0; bj < 2; ++bj)
; #pragma unroll
;                     for (int n = 0; n < 2; ++n)
; #pragma unroll
;                         for (int j = 0; j < 4; ++j) gq[2 * bj + n] = __builtin_amdgcn_cvt_pk_u8_f32(fmaxf(__builtin_rintf(sigmoidf_fast((float)acc[ai][bj][m][n][j] * (r * cs[bj][n][j]) + bg[bj][n][j]) * 255.0f), 1.0f), j, gq[2 * bj + n]);
;                 if (!dry) *(u32x4*)(G + (ai * 4 + m) * 8192) = gq;
;                 ROW_FENCE();
	v_cvt_pk_u8_f32 v151, v47, 3, v151
	s_nop 0
	global_store_dwordx4 v153, v[148:151], s[22:23]
	v_cvt_f32_i32_e32 v24, v24
	v_cvt_f32_i32_e32 v25, v25
	v_cvt_f32_i32_e32 v26, v26
	v_cvt_f32_i32_e32 v27, v27
	v_cvt_f32_i32_e32 v20, v20
	v_cvt_f32_i32_e32 v21, v21
	v_cvt_f32_i32_e32 v22, v22
	v_cvt_f32_i32_e32 v23, v23
	v_pk_mul_f32 v[24:25], v[24:25], v[206:207]
	v_pk_mul_f32 v[26:27], v[26:27], v[208:209]
	v_pk_mul_f32 v[20:21], v[20:21], v[210:211]
	v_pk_mul_f32 v[22:23], v[22:23], v[212:213]
	v_pk_fma_f32 v[24:25], v[24:25], v[244:245], v[222:223] op_sel_hi:[1,0,1]
	v_pk_fma_f32 v[26:27], v[26:27], v[244:245], v[224:225] op_sel_hi:[1,0,1]
	v_pk_fma_f32 v[20:21], v[20:21], v[244:245], v[226:227] op_sel_hi:[1,0,1]
	v_pk_fma_f32 v[22:23], v[22:23], v[244:245], v[228:229] op_sel_hi:[1,0,1]
	v_exp_f32_e32 v24, v24
	v_exp_f32_e32 v25, v25
	v_exp_f32_e32 v26, v26
	v_exp_f32_e32 v27, v27
	v_exp_f32_e32 v20, v20
	v_exp_f32_e32 v21, v21
	v_exp_f32_e32 v22, v22
	v_exp_f32_e32 v23, v23
	v_pk_fma_f32 v[24:25], v[24:25], v[156:157], v[156:157] op_sel_hi:[1,0,0]
	v_pk_fma_f32 v[26:27], v[26:27], v[156:157], v[156:157] op_sel_hi:[1,0,0]
	v_pk_fma_f32 v[20:21], v[20:21], v[156:157], v[156:157] op_sel_hi:[1,0,0]
	v_pk_fma_f32 v[22:23], v[22:23], v[156:157], v[156:157] op_sel_hi:[1,0,0]
	v_rcp_f32_e32 v24, v24
	v_rcp_f32_e32 v25, v25
	v_rcp_f32_e32 v26, v26
	v_rcp_f32_e32 v27, v27
	v_rcp_f32_e32 v20, v20
	v_rcp_f32_e32 v21, v21
	v_rcp_f32_e32 v22, v22
	v_rcp_f32_e32 v23, v23
	v_add_u32_e32 v153, 0xc000, v152
	v_rndne_f32_e32 v24, v24
	v_rndne_f32_e32 v25, v25
	v_rndne_f32_e32 v26, v26
	v_rndne_f32_e32 v27, v27
	v_rndne_f32_e32 v20, v20
	v_rndne_f32_e32 v21, v21
	v_rndne_f32_e32 v22, v22
	v_rndne_f32_e32 v23, v23
	v_max_f32_e32 v24, 1.0, v24
	v_max_f32_e32 v25, 1.0, v25
	v_max_f32_e32 v26, 1.0, v26
	v_max_f32_e32 v27, 1.0, v27
	v_max_f32_e32 v20, 1.0, v20
	v_max_f32_e32 v21, 1.0, v21
	v_max_f32_e32 v22, 1.0, v22
	v_max_f32_e32 v23, 1.0, v23
	v_cvt_pk_u8_f32 v144, v24, 0, 0
	v_cvt_pk_u8_f32 v145, v20, 0, 0
	v_cvt_pk_u8_f32 v144, v25, 1, v144
	v_cvt_pk_u8_f32 v145, v21, 1, v145
	v_cvt_pk_u8_f32 v144, v26, 2, v144
	v_cvt_pk_u8_f32 v145, v22, 2, v145
	v_cvt_pk_u8_f32 v144, v27, 3, v144
	v_cvt_pk_u8_f32 v145, v23, 3, v145
	v_cvt_f32_i32_e32 v16, v16
	v_cvt_f32_i32_e32 v17, v17
	v_cvt_f32_i32_e32 v18, v18
	v_cvt_f32_i32_e32 v19, v19
	v_cvt_f32_i32_e32 v28, v28
	v_cvt_f32_i32_e32 v29, v29
	v_cvt_f32_i32_e32 v30, v30
	v_cvt_f32_i32_e32 v31, v31
	v_pk_mul_f32 v[16:17], v[16:17], v[214:215]
	v_pk_mul_f32 v[18:19], v[18:19], v[216:217]
	v_pk_mul_f32 v[28:29], v[28:29], v[218:219]
	v_pk_mul_f32 v[30:31], v[30:31], v[220:221]
	v_pk_fma_f32 v[16:17], v[16:17], v[244:245], v[230:231] op_sel_hi:[1,0,1]
	v_pk_fma_f32 v[18:19], v[18:19], v[244:245], v[232:233] op_sel_hi:[1,0,1]
	v_pk_fma_f32 v[28:29], v[28:29], v[244:245], v[234:235] op_sel_hi:[1,0,1]
	v_pk_fma_f32 v[30:31], v[30:31], v[244:245], v[236:237] op_sel_hi:[1,0,1]
	v_exp_f32_e32 v16, v16
	v_exp_f32_e32 v17, v17
	v_exp_f32_e32 v18, v18
	v_exp_f32_e32 v19, v19
	v_exp_f32_e32 v28, v28
	v_exp_f32_e32 v29, v29
	v_exp_f32_e32 v30, v30
	v_exp_f32_e32 v31, v31
	v_pk_fma_f32 v[16:17], v[16:17], v[156:157], v[156:157] op_sel_hi:[1,0,0]
	v_pk_fma_f32 v[18:19], v[18:19], v[156:157], v[156:157] op_sel_hi:[1,0,0]
	v_pk_fma_f32 v[28:29], v[28:29], v[156:157], v[156:157] op_sel_hi:[1,0,0]
	v_pk_fma_f32 v[30:31], v[30:31], v[156:157], v[156:157] op_sel_hi:[1,0,0]
	v_rcp_f32_e32 v16, v16
	v_rcp_f32_e32 v17, v17
	v_rcp_f32_e32 v18, v18
	v_rcp_f32_e32 v19, v19
	v_rcp_f32_e32 v28, v28
	v_rcp_f32_e32 v29, v29
	v_rcp_f32_e32 v30, v30
	v_rcp_f32_e32 v31, v31
	s_nop 0
	v_rndne_f32_e32 v16, v16
	v_rndne_f32_e32 v17, v17
	v_rndne_f32_e32 v18, v18
	v_rndne_f32_e32 v19, v19
	v_rndne_f32_e32 v28, v28
	v_rndne_f32_e32 v29, v29
	v_rndne_f32_e32 v30, v30
	v_rndne_f32_e32 v31, v31
	v_max_f32_e32 v16, 1.0, v16
	v_max_f32_e32 v17, 1.0, v17
	v_max_f32_e32 v18, 1.0, v18
	v_max_f32_e32 v19, 1.0, v19
	v_max_f32_e32 v28, 1.0, v28
	v_max_f32_e32 v29, 1.0, v29
	v_max_f32_e32 v30, 1.0, v30
	v_max_f32_e32 v31, 1.0, v31
	v_cvt_pk_u8_f32 v146, v16, 0, 0
	v_cvt_pk_u8_f32 v147, v28, 0, 0
	v_cvt_pk_u8_f32 v146, v17, 1, v146
	v_cvt_pk_u8_f32 v147, v29, 1, v147
	v_cvt_pk_u8_f32 v146, v18, 2, v146
	v_cvt_pk_u8_f32 v147, v30, 2, v147
	v_cvt_pk_u8_f32 v146, v19, 3, v146
	v_cvt_pk_u8_f32 v147, v31, 3, v147
	s_nop 0
	global_store_dwordx4 v153, v[144:147], s[22:23]
; __device__ __forceinline__ float sigmoidf_fast(float x) { return fast_rcp(1.0f + fast_exp2(-x * LOG2E)); }
; #define PG8_BAR __builtin_amdgcn_s_barrier()
; #define ROW_FENCE() asm volatile("" ::: "memory")
; template <class Epi, class Sched, bool ALIGN_EPI = true, bool SP2 = true, bool I8 = false, bool F8 = false>
; __device__ __forceinline__ void gemm_phase(LAS unsigned char* lds, const int K, const Sched& S, const Epi& E, const int wave) {
;     ...
;         if (!has_next) break;
;         if (!(Epi::KEEPS && cur.sub < 2)) {
; #pragma unroll
;         for (int a = 0; a < 2; ++a)
; #pragma unroll
;             for (int b = 0; b < 2; ++b)
; #pragma unroll
;                 for (int m = 0; m < 4; ++m)
; #pragma unroll
;                     for (int n = 0; n < 2; ++n) acc[a][b][m][n] = (acc_t){0, 0, 0, 0};
;         }
;         cur = nxt; cA = nA; cB = nB; ++ui;
;         if constexpr (ALIGN_EPI) { if (wr == 1) PG8_BAR; }
;     __device__ __forceinline__ void operator()(const pg8::i32x4 (&acc)[2][2][4][2], const pg8::Unit& u, int wr, int wc, int fr, int fq) const {
;     ...
;         for (int ai = 0; ai < 2; ++ai)
; #pragma unroll
;             for (int m = 0; m < 4; ++m) {
;                 const int row = u.pm * 256 + ai * 128 + wr * 64 + m * 16 + fr; const float r = rsv[ai][m];
;                 u32x4 gq = {0u, 0u, 0u, 0u};
; #pragma unroll
;                 for (int bj = 0; bj < 2; ++bj)
; #pragma unroll
;                     for (int n = 0; n < 2; ++n)
; #pragma unroll
;                         for (int j = 0; j < 4; ++j) gq[2 * bj + n] = __builtin_amdgcn_cvt_pk_u8_f32(fmaxf(__builtin_rintf(sigmoidf_fast((float)acc[ai][bj][m][n][j] * (r * cs[bj][n][j]) + bg[bj][n][j]) * 255.0f), 1.0f), j, gq[2 * bj + n]);
;                 if (!dry) *(u32x4*)(G + (ai * 4 + m) * 8192) = gq;
;                 ROW_FENCE();
	v_cvt_f32_i32_e32 v8, v8
	v_cvt_f32_i32_e32 v9, v9
	v_cvt_f32_i32_e32 v10, v10
	v_cvt_f32_i32_e32 v11, v11
	v_cvt_f32_i32_e32 v4, v4
	v_cvt_f32_i32_e32 v5, v5
	v_cvt_f32_i32_e32 v6, v6
	v_cvt_f32_i32_e32 v7, v7
	v_pk_mul_f32 v[8:9], v[8:9], v[206:207]
	v_pk_mul_f32 v[10:11], v[10:11], v[208:209]
	v_pk_mul_f32 v[4:5], v[4:5], v[210:211]
	v_pk_mul_f32 v[6:7], v[6:7], v[212:213]
	v_pk_fma_f32 v[8:9], v[8:9], v[244:245], v[222:223] op_sel:[0,1,0] op_sel_hi:[1,1,1]
	v_pk_fma_f32 v[10:11], v[10:11], v[244:245], v[224:225] op_sel:[0,1,0] op_sel_hi:[1,1,1]
	v_pk_fma_f32 v[4:5], v[4:5], v[244:245], v[226:227] op_sel:[0,1,0] op_sel_hi:[1,1,1]
	v_pk_fma_f32 v[6:7], v[6:7], v[244:245], v[228:229] op_sel:[0,1,0] op_sel_hi:[1,1,1]
	v_exp_f32_e32 v8, v8
	v_exp_f32_e32 v9, v9
	v_exp_f32_e32 v10, v10
	v_exp_f32_e32 v11, v11
	v_exp_f32_e32 v4, v4
	v_exp_f32_e32 v5, v5
	v_exp_f32_e32 v6, v6
	v_exp_f32_e32 v7, v7
	v_pk_fma_f32 v[8:9], v[8:9], v[156:157], v[156:157] op_sel_hi:[1,0,0]
	v_pk_fma_f32 v[10:11], v[10:11], v[156:157], v[156:157] op_sel_hi:[1,0,0]
	v_pk_fma_f32 v[4:5], v[4:5], v[156:157], v[156:157] op_sel_hi:[1,0,0]
	v_pk_fma_f32 v[6:7], v[6:7], v[156:157], v[156:157] op_sel_hi:[1,0,0]
	v_rcp_f32_e32 v8, v8
	v_rcp_f32_e32 v9, v9
	v_rcp_f32_e32 v10, v10
	v_rcp_f32_e32 v11, v11
	v_rcp_f32_e32 v4, v4
	v_rcp_f32_e32 v5, v5
	v_rcp_f32_e32 v6, v6
	v_rcp_f32_e32 v7, v7
	v_add_u32_e32 v153, 0xe000, v152
	v_rndne_f32_e32 v8, v8
	v_rndne_f32_e32 v9, v9
	v_rndne_f32_e32 v10, v10
	v_rndne_f32_e32 v11, v11
	v_rndne_f32_e32 v4, v4
	v_rndne_f32_e32 v5, v5
	v_rndne_f32_e32 v6, v6
	v_rndne_f32_e32 v7, v7
	v_max_f32_e32 v8, 1.0, v8
	v_max_f32_e32 v9, 1.0, v9
	v_max_f32_e32 v10, 1.0, v10
	v_max_f32_e32 v11, 1.0, v11
	v_max_f32_e32 v4, 1.0, v4
	v_max_f32_e32 v5, 1.0, v5
	v_max_f32_e32 v6, 1.0, v6
	v_max_f32_e32 v7, 1.0, v7
	v_cvt_pk_u8_f32 v148, v8, 0, 0
	v_cvt_pk_u8_f32 v149, v4, 0, 0
	v_cvt_pk_u8_f32 v148, v9, 1, v148
	v_cvt_pk_u8_f32 v149, v5, 1, v149
	v_cvt_pk_u8_f32 v148, v10, 2, v148
	v_cvt_pk_u8_f32 v149, v6, 2, v149
	v_cvt_pk_u8_f32 v148, v11, 3, v148
	v_cvt_pk_u8_f32 v149, v7, 3, v149
	v_cvt_f32_i32_e32 v0, v0
	v_cvt_f32_i32_e32 v1, v1
	v_cvt_f32_i32_e32 v2, v2
	v_cvt_f32_i32_e32 v3, v3
	v_cvt_f32_i32_e32 v12, v12
	v_cvt_f32_i32_e32 v13, v13
	v_cvt_f32_i32_e32 v14, v14
	v_cvt_f32_i32_e32 v15, v15
	v_pk_mul_f32 v[0:1], v[0:1], v[214:215]
	v_pk_mul_f32 v[2:3], v[2:3], v[216:217]
	v_pk_mul_f32 v[12:13], v[12:13], v[218:219]
	v_pk_mul_f32 v[14:15], v[14:15], v[220:221]
	v_pk_fma_f32 v[0:1], v[0:1], v[244:245], v[230:231] op_sel:[0,1,0] op_sel_hi:[1,1,1]
	v_pk_fma_f32 v[2:3], v[2:3], v[244:245], v[232:233] op_sel:[0,1,0] op_sel_hi:[1,1,1]
	v_pk_fma_f32 v[12:13], v[12:13], v[244:245], v[234:235] op_sel:[0,1,0] op_sel_hi:[1,1,1]
	v_pk_fma_f32 v[14:15], v[14:15], v[244:245], v[236:237] op_sel:[0,1,0] op_sel_hi:[1,1,1]
	v_exp_f32_e32 v0, v0
	v_exp_f32_e32 v1, v1
	v_exp_f32_e32 v2, v2
	v_exp_f32_e32 v3, v3
	v_exp_f32_e32 v12, v12
	v_exp_f32_e32 v13, v13
	v_exp_f32_e32 v14, v14
	v_exp_f32_e32 v15, v15
	v_pk_fma_f32 v[0:1], v[0:1], v[156:157], v[156:157] op_sel_hi:[1,0,0]
	v_pk_fma_f32 v[2:3], v[2:3], v[156:157], v[156:157] op_sel_hi:[1,0,0]
	v_pk_fma_f32 v[12:13], v[12:13], v[156:157], v[156:157] op_sel_hi:[1,0,0]
	v_pk_fma_f32 v[14:15], v[14:15], v[156:157], v[156:157] op_sel_hi:[1,0,0]
	v_rcp_f32_e32 v0, v0
	v_rcp_f32_e32 v1, v1
	v_rcp_f32_e32 v2, v2
	v_rcp_f32_e32 v3, v3
	v_rcp_f32_e32 v12, v12
	v_rcp_f32_e32 v13, v13
	v_rcp_f32_e32 v14, v14
	v_rcp_f32_e32 v15, v15
	s_nop 0
	v_rndne_f32_e32 v0, v0
	v_rndne_f32_e32 v1, v1
	v_rndne_f32_e32 v2, v2
	v_rndne_f32_e32 v3, v3
	v_rndne_f32_e32 v12, v12
	v_rndne_f32_e32 v13, v13
	v_rndne_f32_e32 v14, v14
	v_rndne_f32_e32 v15, v15
	v_max_f32_e32 v0, 1.0, v0
	v_max_f32_e32 v1, 1.0, v1
	v_max_f32_e32 v2, 1.0, v2
	v_max_f32_e32 v3, 1.0, v3
	v_max_f32_e32 v12, 1.0, v12
	v_max_f32_e32 v13, 1.0, v13
	v_max_f32_e32 v14, 1.0, v14
	v_max_f32_e32 v15, 1.0, v15
	v_cvt_pk_u8_f32 v150, v0, 0, 0
	v_cvt_pk_u8_f32 v151, v12, 0, 0
	v_cvt_pk_u8_f32 v150, v1, 1, v150
	v_cvt_pk_u8_f32 v151, v13, 1, v151
	v_cvt_pk_u8_f32 v150, v2, 2, v150
	v_cvt_pk_u8_f32 v151, v14, 2, v151
	v_cvt_pk_u8_f32 v150, v3, 3, v150
	v_cvt_pk_u8_f32 v151, v15, 3, v151
	s_nop 0
	global_store_dwordx4 v153, v[148:151], s[22:23]
	s_andn2_b64 vcc, exec, s[2:3]
	s_mov_b64 s[2:3], -1
	s_cbranch_vccnz .LBB0_442
	s_andn2_b64 vcc, exec, s[0:1]
	s_cbranch_vccnz .LBB0_441
	s_barrier
	s_branch .LBB0_441
